# baseline (speedup 1.0000x reference)
_Z13logits_kernelPKDv8_DF16bS1_PKfS3_PDv2_fS5_Pf:
	s_load_dwordx4 s[4:7], s[0:1], 0x0
	s_load_dwordx4 s[12:15], s[0:1], 0x10
	s_load_dwordx4 s[24:27], s[0:1], 0x20
	s_load_dwordx2 s[28:29], s[0:1], 0x30
	s_lshl_b32 s3, s2, 1
	s_and_b32 s3, s3, 14
	s_ashr_i32 s8, s2, 7
	s_bfe_u32 s10, s2, 0x40003
	s_add_i32 s3, s3, s8
	v_lshrrev_b32_e32 v1, 6, v0
	v_and_b32_e32 v2, 63, v0
	s_movk_i32 s11, 0x3000
	v_lshlrev_b32_e32 v2, 4, v2
	v_and_b32_e32 v5, 31, v0
	v_mad_u32_u24 v2, v1, s11, v2
	v_lshlrev_b32_e32 v5, 2, v5
	s_lshl_b32 s9, s3, 9
	v_add_u32_e32 v3, 0x1000, v2
	v_add_u32_e32 v4, 0x2000, v2
	v_add_u32_e32 v5, s9, v5
	s_mul_i32 s8, s10, 0xc000
	s_mul_i32 s9, s3, 0x30000
	s_waitcnt lgkmcnt(0)
	s_load_dword s22, s[14:15], 0x0
	global_load_dword v248, v5, s[12:13]
	global_load_dword v249, v5, s[12:13] offset:128
	global_load_dword v250, v5, s[12:13] offset:256
	global_load_dword v251, v5, s[12:13] offset:384
	s_add_u32 s4, s4, s8
	s_addc_u32 s5, s5, 0
	s_add_u32 s6, s6, s9
	s_addc_u32 s7, s7, 0
	s_add_u32 s16, s6, 0xc000
	s_addc_u32 s17, s7, 0
	s_add_u32 s18, s6, 0x18000
	s_addc_u32 s19, s7, 0
	s_add_u32 s20, s6, 0x24000
	s_addc_u32 s21, s7, 0
	s_cmp_eq_u32 s10, 0
	s_cbranch_scc1 .Llg_lead
	s_sleep 6
.Llg_lead:
	global_load_dwordx4 v[8:11], v2, s[4:5]
	global_load_dwordx4 v[56:59], v2, s[6:7]
	global_load_dwordx4 v[104:107], v2, s[16:17]
	global_load_dwordx4 v[152:155], v2, s[18:19]
	global_load_dwordx4 v[200:203], v2, s[20:21]
	global_load_dwordx4 v[12:15], v2, s[4:5] offset:1024
	global_load_dwordx4 v[60:63], v2, s[6:7] offset:1024
	global_load_dwordx4 v[108:111], v2, s[16:17] offset:1024
	global_load_dwordx4 v[156:159], v2, s[18:19] offset:1024
	global_load_dwordx4 v[204:207], v2, s[20:21] offset:1024
	global_load_dwordx4 v[16:19], v2, s[4:5] offset:2048
	global_load_dwordx4 v[64:67], v2, s[6:7] offset:2048
	global_load_dwordx4 v[112:115], v2, s[16:17] offset:2048
	global_load_dwordx4 v[160:163], v2, s[18:19] offset:2048
	global_load_dwordx4 v[208:211], v2, s[20:21] offset:2048
	global_load_dwordx4 v[20:23], v2, s[4:5] offset:3072
	global_load_dwordx4 v[68:71], v2, s[6:7] offset:3072
	global_load_dwordx4 v[116:119], v2, s[16:17] offset:3072
	global_load_dwordx4 v[164:167], v2, s[18:19] offset:3072
	global_load_dwordx4 v[212:215], v2, s[20:21] offset:3072
	global_load_dwordx4 v[24:27], v3, s[4:5]
	global_load_dwordx4 v[72:75], v3, s[6:7]
	global_load_dwordx4 v[120:123], v3, s[16:17]
	global_load_dwordx4 v[168:171], v3, s[18:19]
	global_load_dwordx4 v[216:219], v3, s[20:21]
	global_load_dwordx4 v[28:31], v3, s[4:5] offset:1024
	global_load_dwordx4 v[76:79], v3, s[6:7] offset:1024
	global_load_dwordx4 v[124:127], v3, s[16:17] offset:1024
	global_load_dwordx4 v[172:175], v3, s[18:19] offset:1024
	global_load_dwordx4 v[220:223], v3, s[20:21] offset:1024
	global_load_dwordx4 v[32:35], v3, s[4:5] offset:2048
	global_load_dwordx4 v[80:83], v3, s[6:7] offset:2048
	global_load_dwordx4 v[128:131], v3, s[16:17] offset:2048
	global_load_dwordx4 v[176:179], v3, s[18:19] offset:2048
	global_load_dwordx4 v[224:227], v3, s[20:21] offset:2048
	global_load_dwordx4 v[36:39], v3, s[4:5] offset:3072
	global_load_dwordx4 v[84:87], v3, s[6:7] offset:3072
	global_load_dwordx4 v[132:135], v3, s[16:17] offset:3072
	global_load_dwordx4 v[180:183], v3, s[18:19] offset:3072
	global_load_dwordx4 v[228:231], v3, s[20:21] offset:3072
	global_load_dwordx4 v[40:43], v4, s[4:5]
	global_load_dwordx4 v[88:91], v4, s[6:7]
	global_load_dwordx4 v[136:139], v4, s[16:17]
	global_load_dwordx4 v[184:187], v4, s[18:19]
	global_load_dwordx4 v[232:235], v4, s[20:21]
	global_load_dwordx4 v[44:47], v4, s[4:5] offset:1024
	global_load_dwordx4 v[92:95], v4, s[6:7] offset:1024
	global_load_dwordx4 v[140:143], v4, s[16:17] offset:1024
	global_load_dwordx4 v[188:191], v4, s[18:19] offset:1024
	global_load_dwordx4 v[236:239], v4, s[20:21] offset:1024
	global_load_dwordx4 v[48:51], v4, s[4:5] offset:2048
	global_load_dwordx4 v[96:99], v4, s[6:7] offset:2048
	global_load_dwordx4 v[144:147], v4, s[16:17] offset:2048
	global_load_dwordx4 v[192:195], v4, s[18:19] offset:2048
	global_load_dwordx4 v[240:243], v4, s[20:21] offset:2048
	global_load_dwordx4 v[52:55], v4, s[4:5] offset:3072
	global_load_dwordx4 v[100:103], v4, s[6:7] offset:3072
	global_load_dwordx4 v[148:151], v4, s[16:17] offset:3072
	global_load_dwordx4 v[196:199], v4, s[18:19] offset:3072
	global_load_dwordx4 v[244:247], v4, s[20:21] offset:3072
	s_waitcnt vmcnt(58)
	v_mfma_f32_32x32x16_bf16 a[0:15], v[8:11], v[56:59], 0
	s_waitcnt vmcnt(57)
	v_mfma_f32_32x32x16_bf16 a[0:15], v[8:11], v[104:107], a[0:15]
	s_waitcnt vmcnt(56)
	v_mfma_f32_32x32x16_bf16 a[0:15], v[8:11], v[152:155], a[0:15]
	s_waitcnt vmcnt(55)
	v_mfma_f32_32x32x16_bf16 a[0:15], v[8:11], v[200:203], a[0:15]
	s_waitcnt vmcnt(53)
	v_mfma_f32_32x32x16_bf16 a[0:15], v[12:15], v[60:63], a[0:15]
	s_waitcnt vmcnt(52)
	v_mfma_f32_32x32x16_bf16 a[0:15], v[12:15], v[108:111], a[0:15]
	s_waitcnt vmcnt(51)
	v_mfma_f32_32x32x16_bf16 a[0:15], v[12:15], v[156:159], a[0:15]
	s_waitcnt vmcnt(50)
	v_mfma_f32_32x32x16_bf16 a[0:15], v[12:15], v[204:207], a[0:15]
	s_waitcnt vmcnt(48)
	v_mfma_f32_32x32x16_bf16 a[0:15], v[16:19], v[64:67], a[0:15]
	s_waitcnt vmcnt(47)
	v_mfma_f32_32x32x16_bf16 a[0:15], v[16:19], v[112:115], a[0:15]
	s_waitcnt vmcnt(46)
	v_mfma_f32_32x32x16_bf16 a[0:15], v[16:19], v[160:163], a[0:15]
	s_waitcnt vmcnt(45)
	v_mfma_f32_32x32x16_bf16 a[0:15], v[16:19], v[208:211], a[0:15]
	s_waitcnt vmcnt(43)
	v_mfma_f32_32x32x16_bf16 a[0:15], v[20:23], v[68:71], a[0:15]
	s_waitcnt vmcnt(42)
	v_mfma_f32_32x32x16_bf16 a[0:15], v[20:23], v[116:119], a[0:15]
	s_waitcnt vmcnt(41)
	v_mfma_f32_32x32x16_bf16 a[0:15], v[20:23], v[164:167], a[0:15]
	s_waitcnt vmcnt(40)
	v_mfma_f32_32x32x16_bf16 a[0:15], v[20:23], v[212:215], a[0:15]
	s_waitcnt vmcnt(38)
	v_mfma_f32_32x32x16_bf16 a[0:15], v[24:27], v[72:75], a[0:15]
	s_waitcnt vmcnt(37)
	v_mfma_f32_32x32x16_bf16 a[0:15], v[24:27], v[120:123], a[0:15]
	s_waitcnt vmcnt(36)
	v_mfma_f32_32x32x16_bf16 a[0:15], v[24:27], v[168:171], a[0:15]
	s_waitcnt vmcnt(35)
	v_mfma_f32_32x32x16_bf16 a[0:15], v[24:27], v[216:219], a[0:15]
	s_waitcnt vmcnt(33)
	v_mfma_f32_32x32x16_bf16 a[0:15], v[28:31], v[76:79], a[0:15]
	s_waitcnt vmcnt(32)
	v_mfma_f32_32x32x16_bf16 a[0:15], v[28:31], v[124:127], a[0:15]
	s_waitcnt vmcnt(31)
	v_mfma_f32_32x32x16_bf16 a[0:15], v[28:31], v[172:175], a[0:15]
	s_waitcnt vmcnt(30)
	v_mfma_f32_32x32x16_bf16 a[0:15], v[28:31], v[220:223], a[0:15]
	s_waitcnt vmcnt(28)
	v_mfma_f32_32x32x16_bf16 a[0:15], v[32:35], v[80:83], a[0:15]
	s_waitcnt vmcnt(27)
	v_mfma_f32_32x32x16_bf16 a[0:15], v[32:35], v[128:131], a[0:15]
	s_waitcnt vmcnt(26)
	v_mfma_f32_32x32x16_bf16 a[0:15], v[32:35], v[176:179], a[0:15]
	s_waitcnt vmcnt(25)
	v_mfma_f32_32x32x16_bf16 a[0:15], v[32:35], v[224:227], a[0:15]
	s_waitcnt vmcnt(23)
	v_mfma_f32_32x32x16_bf16 a[0:15], v[36:39], v[84:87], a[0:15]
	s_waitcnt vmcnt(22)
	v_mfma_f32_32x32x16_bf16 a[0:15], v[36:39], v[132:135], a[0:15]
	s_waitcnt vmcnt(21)
	v_mfma_f32_32x32x16_bf16 a[0:15], v[36:39], v[180:183], a[0:15]
	s_waitcnt vmcnt(20)
	v_mfma_f32_32x32x16_bf16 a[0:15], v[36:39], v[228:231], a[0:15]
	s_waitcnt vmcnt(18)
	v_mfma_f32_32x32x16_bf16 a[0:15], v[40:43], v[88:91], a[0:15]
	s_waitcnt vmcnt(17)
	v_mfma_f32_32x32x16_bf16 a[0:15], v[40:43], v[136:139], a[0:15]
	s_waitcnt vmcnt(16)
	v_mfma_f32_32x32x16_bf16 a[0:15], v[40:43], v[184:187], a[0:15]
	s_waitcnt vmcnt(15)
	v_mfma_f32_32x32x16_bf16 a[0:15], v[40:43], v[232:235], a[0:15]
	s_waitcnt vmcnt(13)
	v_mfma_f32_32x32x16_bf16 a[0:15], v[44:47], v[92:95], a[0:15]
	s_waitcnt vmcnt(12)
	v_mfma_f32_32x32x16_bf16 a[0:15], v[44:47], v[140:143], a[0:15]
	s_waitcnt vmcnt(11)
	v_mfma_f32_32x32x16_bf16 a[0:15], v[44:47], v[188:191], a[0:15]
	s_waitcnt vmcnt(10)
	v_mfma_f32_32x32x16_bf16 a[0:15], v[44:47], v[236:239], a[0:15]
	v_add_f32_e32 v8, 0, v248
	v_add_f32_e32 v8, v8, v249
	v_add_f32_e32 v8, v8, v250
	v_add_f32_e32 v8, v8, v251
	v_mov_b32_e32 v9, 0x3fb8aa3b
	s_waitcnt lgkmcnt(0)
	v_mul_f32_e32 v9, s22, v9
	v_exp_f32_e32 v9, v9
	v_add_f32_e32 v10, 0x2b8cbccc, v8
	v_div_scale_f32 v11, s[8:9], v10, v10, v9
	v_rcp_f32_e32 v12, v11
	v_div_scale_f32 v13, vcc, v9, v10, v9
	v_fma_f32 v14, -v11, v12, 1.0
	v_fmac_f32_e32 v12, v14, v12
	v_mul_f32_e32 v14, v13, v12
	v_fma_f32 v15, -v11, v14, v13
	v_fmac_f32_e32 v14, v15, v12
	v_fma_f32 v11, -v11, v14, v13
	v_div_fmas_f32 v11, v11, v12, v14
	v_div_fixup_f32 v9, v11, v10, v9
	v_lshlrev_b32_e32 v10, 2, v0
	v_add_u32_e32 v10, 0x4000, v10
	v_cmp_gt_u32_e32 vcc, 32, v0
	s_and_saveexec_b64 s[8:9], vcc
	ds_write2_b32 v10, v8, v9 offset0:128 offset1:160
	s_mov_b64 exec, s[8:9]
	s_waitcnt vmcnt(8)
	v_mfma_f32_32x32x16_bf16 a[0:15], v[48:51], v[96:99], a[0:15]
	s_waitcnt vmcnt(7)
	v_mfma_f32_32x32x16_bf16 a[0:15], v[48:51], v[144:147], a[0:15]
	s_waitcnt vmcnt(6)
	v_mfma_f32_32x32x16_bf16 a[0:15], v[48:51], v[192:195], a[0:15]
	s_waitcnt vmcnt(5)
	v_mfma_f32_32x32x16_bf16 a[0:15], v[48:51], v[240:243], a[0:15]
	v_mul_u32_u24_e32 v1, 0x1080, v1
	s_movk_i32 s4, 0x7f
	s_movk_i32 s6, 0x84
	v_cmp_lt_u32_e32 vcc, s4, v0
	v_lshrrev_b32_e32 v11, 3, v0
	v_and_b32_e32 v10, 31, v0
	v_and_b32_e32 v11, 4, v11
	v_mul_u32_u24_e32 v11, 0x84, v11
	v_lshlrev_b32_e32 v9, 2, v10
	v_bfe_u32 v6, v0, 2, 5
	v_and_b32_e32 v7, 3, v0
	v_add3_u32 v1, v1, v11, v9
	v_lshlrev_b32_e32 v8, 3, v7
	s_waitcnt vmcnt(3)
	v_mfma_f32_32x32x16_bf16 a[0:15], v[52:55], v[100:103], a[0:15]
	s_waitcnt vmcnt(2)
	v_mfma_f32_32x32x16_bf16 a[0:15], v[52:55], v[148:151], a[0:15]
	s_waitcnt vmcnt(1)
	v_mfma_f32_32x32x16_bf16 a[0:15], v[52:55], v[196:199], a[0:15]
	s_waitcnt vmcnt(0)
	v_mfma_f32_32x32x16_bf16 a[0:15], v[52:55], v[244:247], a[0:15]
	s_nop 11
	ds_write_b32 v1, a0
	ds_write_b32 v1, a1 offset:132
	ds_write_b32 v1, a2 offset:264
	ds_write_b32 v1, a3 offset:396
	ds_write_b32 v1, a4 offset:1056
	ds_write_b32 v1, a5 offset:1188
	ds_write_b32 v1, a6 offset:1320
	ds_write_b32 v1, a7 offset:1452
	ds_write_b32 v1, a8 offset:2112
	ds_write_b32 v1, a9 offset:2244
	ds_write_b32 v1, a10 offset:2376
	ds_write_b32 v1, a11 offset:2508
	ds_write_b32 v1, a12 offset:3168
	ds_write_b32 v1, a13 offset:3300
	ds_write_b32 v1, a14 offset:3432
	ds_write_b32 v1, a15 offset:3564
	v_bfe_u32 v6, v0, 2, 5
	v_and_b32_e32 v7, 3, v0
	v_lshlrev_b32_e32 v9, 3, v7
	v_readfirstlane_b32 s30, v0
	v_sub_u32_e32 v10, v6, v9
	s_waitcnt lgkmcnt(0)
	s_barrier
	s_cmpk_ge_u32 s30, 0x80
	s_cbranch_scc1 .Llg_k1
	v_mul_u32_u24_e32 v2, 0x84, v6
	v_lshlrev_b32_e32 v8, 5, v7
	v_add_u32_e32 v2, v2, v8
	v_add_u32_e32 v8, 0x4280, v8
	v_add_u32_e32 v3, 0x1080, v2
	v_add_u32_e32 v4, 0x2100, v2
	v_add_u32_e32 v5, 0x3180, v2
	ds_read_b128 v[48:51], v8
	ds_read_b128 v[52:55], v8 offset:16
	ds_read2_b32 v[16:17], v2 offset0:0 offset1:1
	ds_read2_b32 v[18:19], v2 offset0:2 offset1:3
	ds_read2_b32 v[20:21], v2 offset0:4 offset1:5
	ds_read2_b32 v[22:23], v2 offset0:6 offset1:7
	ds_read2_b32 v[24:25], v3 offset0:0 offset1:1
	ds_read2_b32 v[26:27], v3 offset0:2 offset1:3
	ds_read2_b32 v[28:29], v3 offset0:4 offset1:5
	ds_read2_b32 v[30:31], v3 offset0:6 offset1:7
	ds_read2_b32 v[32:33], v4 offset0:0 offset1:1
	ds_read2_b32 v[34:35], v4 offset0:2 offset1:3
	ds_read2_b32 v[36:37], v4 offset0:4 offset1:5
	ds_read2_b32 v[38:39], v4 offset0:6 offset1:7
	s_waitcnt lgkmcnt(4)
	ds_read2_b32 v[40:41], v5 offset0:0 offset1:1
	ds_read2_b32 v[42:43], v5 offset0:2 offset1:3
	ds_read2_b32 v[44:45], v5 offset0:4 offset1:5
	ds_read2_b32 v[46:47], v5 offset0:6 offset1:7
	s_waitcnt lgkmcnt(0)
	s_branch .Llg_join
